# MLA background weight-conversion: store deferred 3+ tiles after its loads, dynamic vmcnt at tile ends
# baseline (speedup 1.0000x reference)
.LBB0_692:
	s_mov_b32 s77, s93
	s_add_i32 s58, s36, 0x3400
	s_add_i32 s59, s36, 0x2000
	s_add_i32 s38, s51, s83
	s_lshl_b64 s[8:9], s[76:77], 26
	s_add_u32 s39, s30, s8
	v_writelane_b32 v252, s40, 23
	s_addc_u32 s40, s28, s9
	s_add_u32 s41, s31, s8
	s_addc_u32 s42, s29, s9
	s_add_u32 s43, s35, s8
	s_addc_u32 s44, s34, s9
	s_add_u32 s45, s27, 0x80000
	s_addc_u32 s46, s26, 0
	s_add_u32 s47, s27, 0x3f200000
	s_addc_u32 s48, s26, 0
	s_add_i32 s49, s76, 1
	s_cmp_eq_u32 s76, 3
	s_mov_b32 s8, 0xa000
	s_cselect_b32 s50, 0x6000, s8
	s_lshl_b32 s61, s51, 5
	s_ashr_i32 s8, s61, 31
	s_add_u32 s22, s27, 0x1ae00000
	s_addc_u32 s23, s26, 0
	v_and_b32_e32 v204, 31, v2
	v_and_b32_e32 v9, 16, v2
	v_lshlrev_b32_e32 v10, 2, v2
	s_add_u32 s62, s27, 0x20e00000
	v_lshrrev_b32_e32 v5, 5, v4
	v_mul_u32_u24_e32 v6, 0xd0, v204
	v_lshlrev_b32_e32 v8, 4, v2
	v_and_or_b32 v9, v10, 12, v9
	s_addc_u32 s63, s26, 0
	v_lshl_add_u32 v205, v5, 4, v6
	v_lshlrev_b32_e32 v6, 8, v5
	v_and_b32_e32 v8, 0xc0, v8
	v_lshlrev_b32_e32 v9, 1, v9
	s_add_u32 s51, s27, 0x43200000
	v_and_b32_e32 v7, 15, v2
	v_or3_b32 v206, v6, v8, v9
	s_waitcnt vmcnt(6)
	s_barrier
	v_mov_b32_e32 v189, s8
	v_lshlrev_b32_e32 v6, 3, v5
	s_addc_u32 s52, s26, 0
	v_lshrrev_b32_e32 v2, 1, v2
	v_cmp_gt_u32_e64 s[8:9], 16, v4
	v_lshlrev_b32_e32 v8, 2, v5
	v_mov_b32_e32 v4, v3
	v_mov_b32_e32 v5, v3
	v_and_b32_e32 v178, 24, v2
	s_add_u32 s24, s27, 0x2f200000
	v_mov_b32_e32 v2, v3
	v_mov_b64_e32 v[100:101], v[4:5]
	s_mov_b32 s60, 3
	v_or_b32_e32 v188, s61, v204
	v_lshlrev_b32_e32 v199, 11, v7
	v_mov_b32_e32 v179, v3
	v_lshlrev_b32_e32 v180, 2, v7
	s_addc_u32 s25, s26, 0
	v_or_b32_e32 v207, 59, v8
	v_mov_b32_e32 v102, v3
	v_mov_b32_e32 v103, v3
	v_mov_b32_e32 v104, v3
	v_mov_b32_e32 v105, v3
	v_mov_b32_e32 v106, v3
	v_mov_b32_e32 v107, v3
	v_mov_b32_e32 v108, v3
	v_mov_b32_e32 v109, v3
	v_mov_b32_e32 v110, v3
	v_mov_b32_e32 v111, v3
	v_mov_b32_e32 v112, v3
	v_mov_b32_e32 v113, v3
	v_mov_b32_e32 v114, v3
	v_mov_b32_e32 v115, v3
	v_mov_b32_e32 v116, v3
	v_mov_b32_e32 v117, v3
	v_mov_b32_e32 v118, v3
	v_mov_b32_e32 v119, v3
	v_mov_b32_e32 v120, v3
	v_mov_b32_e32 v121, v3
	v_mov_b32_e32 v122, v3
	v_mov_b32_e32 v123, v3
	v_mov_b32_e32 v124, v3
	v_mov_b32_e32 v125, v3
	v_mov_b32_e32 v126, v3
	v_mov_b32_e32 v127, v3
	v_mov_b32_e32 v128, v3
	v_mov_b32_e32 v129, v3
	v_mov_b32_e32 v130, v3
	v_mov_b32_e32 v131, v3
	v_mov_b32_e32 v132, v3
	v_mov_b32_e32 v133, v3
	v_mov_b64_e32 v[186:187], 0
	s_mov_b32 s64, 0
	v_lshlrev_b32_e32 v190, 1, v6
	v_lshlrev_b32_e32 v192, 1, v8
	v_readlane_b32 s65, v252, 28
	v_readlane_b32 s66, v252, 26
	v_readlane_b32 s67, v252, 18
	s_mov_b32 s69, 0
	s_mov_b32 s99, 0
	s_mov_b32 s70, 0
	v_mov_b64_e32 v[98:99], v[2:3]
	v_mov_b64_e32 v[184:185], 0
	v_mov_b64_e32 v[182:183], 0
	s_mov_b32 s68, 0
	s_mov_b32 s53, 0
	s_cmp_lt_u32 s61, 0x80
	s_cbranch_scc1 .Lprio_skip
	s_setprio 1

.LBB0_695:
	v_add_f32_e32 v2, v208, v2
	v_add_f32_e32 v2, 0, v2
	v_add_f32_e32 v4, v209, v66
	v_add_f32_e32 v2, v4, v2
	v_add_f32_e32 v4, v84, v67
	v_add_f32_e32 v2, v4, v2
	v_add_f32_e32 v4, v85, v68
	v_add_f32_e32 v2, v4, v2
	v_add_f32_e32 v4, v86, v69
	v_add_f32_e32 v2, v4, v2
	v_add_f32_e32 v4, v87, v70
	v_add_f32_e32 v2, v4, v2
	v_add_f32_e32 v4, v88, v71
	v_add_f32_e32 v2, v4, v2
	v_add_f32_e32 v4, v89, v72
	v_add_f32_e32 v2, v4, v2
	v_add_f32_e32 v4, v90, v73
	v_add_f32_e32 v2, v4, v2
	v_add_f32_e32 v4, v91, v74
	v_add_f32_e32 v2, v4, v2
	v_add_f32_e32 v4, v95, v75
	v_add_f32_e32 v2, v4, v2
	v_add_f32_e32 v4, v77, v82
	v_add_f32_e32 v2, v4, v2
	v_add_f32_e32 v4, v76, v83
	v_add_f32_e32 v2, v4, v2
	v_add_f32_e32 v4, v96, v94
	v_add_f32_e32 v2, v4, v2
	v_add_f32_e32 v4, v79, v93
	s_add_i32 s10, s60, 1
	v_add_f32_e32 v2, v4, v2
	v_add_f32_e32 v4, v78, v92
	s_and_b32 s60, s10, 3
	s_cmp_gt_u32 s99, 1
	s_cbranch_scc1 .Lbgw_f15
	s_waitcnt vmcnt(6) lgkmcnt(0)
	s_branch .Lbgw_fj
.Lbgw_f15:
	s_waitcnt vmcnt(15) lgkmcnt(0)
	s_add_i32 s99, s99, -1
.Lbgw_fj:
	s_barrier
	s_add_i32 s10, s64, 1
	v_add_f32_e32 v2, v4, v2
	s_and_b32 s64, s10, 3
	s_add_i32 s73, s73, 1
	v_add_f32_e32 v191, v191, v2
	s_cmp_eq_u32 s99, 1
	s_cbranch_scc0 .Lbg_nohook
	s_mov_b32 s99, 0
	s_mov_b32 s98, 0
	s_branch .Lbgstore
.Lbg_hookret:
.Lbg_nohook:
	s_cmp_eq_u32 s71, s73
	s_cbranch_scc1 .LBB0_741

.Lbg_pad2:
	global_load_dwordx4 v[98:101], v[186:187], off
	s_branch .LBB0_716
.LBB0_717:
	s_waitcnt lgkmcnt(3)
	v_mov_b64_e32 v[182:183], v[6:7]
	global_load_dwordx4 v[98:101], v[6:7], off
.LBB0_718:
	s_waitcnt lgkmcnt(1)
	v_or_b32_e32 v10, s92, v178
	v_lshlrev_b32_e32 v2, 2, v180
	v_lshl_add_u64 v[4:5], v[4:5], 0, v[2:3]
	v_mul_hi_u32_u24_e32 v7, s28, v10
	v_mul_u32_u24_e32 v6, s28, v10
	v_or_b32_e32 v2, 1, v10
	v_lshl_add_u64 v[6:7], v[6:7], 2, v[4:5]
	v_mul_hi_u32_u24_e32 v9, s28, v2
	v_mul_u32_u24_e32 v8, s28, v2
	v_or_b32_e32 v2, 2, v10
	v_lshl_add_u64 v[8:9], v[8:9], 2, v[4:5]
	global_load_dwordx4 v[102:105], v[6:7], off
	global_load_dwordx4 v[106:109], v[8:9], off
	v_mul_hi_u32_u24_e32 v7, s28, v2
	v_mul_u32_u24_e32 v6, s28, v2
	v_or_b32_e32 v2, 3, v10
	v_lshl_add_u64 v[6:7], v[6:7], 2, v[4:5]
	v_mul_hi_u32_u24_e32 v9, s28, v2
	v_mul_u32_u24_e32 v8, s28, v2
	v_or_b32_e32 v2, 4, v10
	v_lshl_add_u64 v[8:9], v[8:9], 2, v[4:5]
	global_load_dwordx4 v[110:113], v[6:7], off
	global_load_dwordx4 v[114:117], v[8:9], off
	v_mul_hi_u32_u24_e32 v7, s28, v2
	v_mul_u32_u24_e32 v6, s28, v2
	v_or_b32_e32 v2, 5, v10
	v_lshl_add_u64 v[6:7], v[6:7], 2, v[4:5]
	v_mul_hi_u32_u24_e32 v9, s28, v2
	v_mul_u32_u24_e32 v8, s28, v2
	v_or_b32_e32 v2, 6, v10
	v_lshl_add_u64 v[8:9], v[8:9], 2, v[4:5]
	global_load_dwordx4 v[118:121], v[6:7], off
	global_load_dwordx4 v[122:125], v[8:9], off
	v_mul_hi_u32_u24_e32 v7, s28, v2
	v_mul_u32_u24_e32 v6, s28, v2
	v_or_b32_e32 v2, 7, v10
	v_lshl_add_u64 v[6:7], v[6:7], 2, v[4:5]
	v_mul_hi_u32_u24_e32 v9, s28, v2
	v_mul_u32_u24_e32 v8, s28, v2
	v_lshl_add_u64 v[4:5], v[8:9], 2, v[4:5]
	global_load_dwordx4 v[126:129], v[6:7], off
	global_load_dwordx4 v[130:133], v[4:5], off
	s_add_i32 s53, s53, 1
	s_mov_b32 s99, 4

.LBB0_726:
	v_exp_f32_e32 v2, v82
	v_exp_f32_e32 v208, v66
	v_exp_f32_e32 v66, v83
	v_exp_f32_e32 v209, v67
	v_exp_f32_e32 v67, v84
	v_exp_f32_e32 v84, v68
	v_exp_f32_e32 v68, v85
	v_exp_f32_e32 v85, v69
	v_exp_f32_e32 v69, v86
	v_exp_f32_e32 v86, v70
	v_exp_f32_e32 v70, v87
	v_exp_f32_e32 v87, v71
	v_exp_f32_e32 v71, v88
	v_exp_f32_e32 v88, v72
	v_exp_f32_e32 v72, v89
	v_cvt_pk_bf16_f32 v194, v2, v66
	v_cvt_pk_bf16_f32 v195, v67, v68
	v_cvt_pk_bf16_f32 v196, v69, v70
	v_cvt_pk_bf16_f32 v197, v71, v72
	v_exp_f32_e32 v89, v73
	v_exp_f32_e32 v73, v90
	v_mfma_f32_32x32x16_bf16 v[34:49], v[174:177], v[194:197], v[34:49]
	v_exp_f32_e32 v90, v74
	v_exp_f32_e32 v74, v91
	v_exp_f32_e32 v91, v75
	v_exp_f32_e32 v75, v92
	v_exp_f32_e32 v82, v93
	v_exp_f32_e32 v83, v94
	v_exp_f32_e32 v94, v95
	v_mfma_f32_32x32x16_bf16 v[18:33], v[162:165], v[194:197], v[18:33]
	v_exp_f32_e32 v93, v96
	v_exp_f32_e32 v92, v97
	v_cvt_pk_bf16_f32 v174, v73, v74
	v_cvt_pk_bf16_f32 v175, v75, v82
	v_cvt_pk_bf16_f32 v176, v83, v94
	v_cvt_pk_bf16_f32 v177, v93, v92
	v_exp_f32_e32 v95, v76
	v_exp_f32_e32 v77, v77
	v_mfma_f32_32x32x16_bf16 v[34:49], v[170:173], v[174:177], v[34:49]
	v_cvt_pk_bf16_f32 v170, v208, v209
	v_cvt_pk_bf16_f32 v171, v84, v85
	v_cvt_pk_bf16_f32 v172, v86, v87
	v_cvt_pk_bf16_f32 v173, v88, v89
	v_exp_f32_e32 v76, v78
	v_exp_f32_e32 v96, v79
	v_exp_f32_e32 v79, v80
	v_mfma_f32_32x32x16_bf16 v[18:33], v[158:161], v[174:177], v[18:33]
	v_exp_f32_e32 v78, v81
	s_and_b64 vcc, exec, s[10:11]
	v_mfma_f32_32x32x16_bf16 v[34:49], v[166:169], v[170:173], v[34:49]
	v_cvt_pk_bf16_f32 v166, v90, v91
	v_cvt_pk_bf16_f32 v167, v95, v77
	v_cvt_pk_bf16_f32 v168, v76, v96
	v_cvt_pk_bf16_f32 v169, v79, v78
	v_mfma_f32_32x32x16_bf16 v[18:33], v[12:15], v[170:173], v[18:33]
	s_nop 0
	v_mfma_f32_32x32x16_bf16 v[34:49], v[8:11], v[166:169], v[34:49]
	v_mfma_f32_32x32x16_bf16 v[18:33], v[4:7], v[166:169], v[18:33]
	s_branch .LBB0_695
.Lbgstore:
	s_mov_b64 s[28:29], -1
	s_mov_b64 s[10:11], 0
	s_cmp_lt_i32 s70, 1
	s_mov_b64 s[26:27], 0
	s_cbranch_scc0 .LBB0_732
	s_and_b64 vcc, exec, s[28:29]
	s_cbranch_vccnz .LBB0_735

.LBB0_732:
	s_cmp_eq_u32 s70, 1
	s_mov_b64 s[26:27], -1
	s_cbranch_scc0 .LBB0_734
	v_bfe_u32 v4, v102, 16, 1
	v_add3_u32 v4, v102, v4, s86
	v_bfe_u32 v5, v106, 16, 1
	v_lshrrev_b32_e32 v4, 16, v4
	v_add3_u32 v5, v106, v5, s86
	v_and_or_b32 v4, v5, s87, v4
	v_bfe_u32 v5, v110, 16, 1
	v_add3_u32 v5, v110, v5, s86
	v_bfe_u32 v6, v114, 16, 1
	v_lshrrev_b32_e32 v5, 16, v5
	v_add3_u32 v6, v114, v6, s86
	v_and_or_b32 v5, v6, s87, v5
	v_bfe_u32 v6, v118, 16, 1
	v_add3_u32 v6, v118, v6, s86
	v_bfe_u32 v7, v122, 16, 1
	v_lshrrev_b32_e32 v6, 16, v6
	v_add3_u32 v7, v122, v7, s86
	v_and_or_b32 v6, v7, s87, v6
	v_bfe_u32 v7, v126, 16, 1
	v_add3_u32 v7, v126, v7, s86
	v_bfe_u32 v8, v130, 16, 1
	v_lshrrev_b32_e32 v7, 16, v7
	v_add3_u32 v8, v130, v8, s86
	v_and_or_b32 v7, v8, s87, v7
	global_store_dwordx4 v[182:183], v[4:7], off
	v_bfe_u32 v8, v131, 16, 1
	v_add3_u32 v8, v131, v8, s86
	v_bfe_u32 v4, v103, 16, 1
	v_add3_u32 v4, v103, v4, s86
	v_bfe_u32 v5, v107, 16, 1
	v_lshrrev_b32_e32 v4, 16, v4
	v_add3_u32 v5, v107, v5, s86
	v_and_or_b32 v4, v5, s87, v4
	v_bfe_u32 v5, v111, 16, 1
	v_add3_u32 v5, v111, v5, s86
	v_bfe_u32 v6, v115, 16, 1
	v_lshrrev_b32_e32 v5, 16, v5
	v_add3_u32 v6, v115, v6, s86
	v_and_or_b32 v5, v6, s87, v5
	v_bfe_u32 v6, v119, 16, 1
	v_add3_u32 v6, v119, v6, s86
	v_bfe_u32 v7, v123, 16, 1
	v_lshrrev_b32_e32 v6, 16, v6
	v_add3_u32 v7, v123, v7, s86
	v_and_or_b32 v6, v7, s87, v6
	v_bfe_u32 v7, v127, 16, 1
	v_add3_u32 v7, v127, v7, s86
	v_lshrrev_b32_e32 v7, 16, v7
	v_and_or_b32 v7, v8, s87, v7
	global_store_dwordx4 v[182:183], v[4:7], off offset:1024
	v_bfe_u32 v8, v132, 16, 1
	v_add3_u32 v8, v132, v8, s86
	v_bfe_u32 v4, v104, 16, 1
	v_add3_u32 v4, v104, v4, s86
	v_bfe_u32 v5, v108, 16, 1
	v_lshrrev_b32_e32 v4, 16, v4
	v_add3_u32 v5, v108, v5, s86
	v_and_or_b32 v4, v5, s87, v4
	v_bfe_u32 v5, v112, 16, 1
	v_add3_u32 v5, v112, v5, s86
	v_bfe_u32 v6, v116, 16, 1
	v_lshrrev_b32_e32 v5, 16, v5
	v_add3_u32 v6, v116, v6, s86
	v_and_or_b32 v5, v6, s87, v5
	v_bfe_u32 v6, v120, 16, 1
	v_add3_u32 v6, v120, v6, s86
	v_bfe_u32 v7, v124, 16, 1
	v_lshrrev_b32_e32 v6, 16, v6
	v_add3_u32 v7, v124, v7, s86
	v_and_or_b32 v6, v7, s87, v6
	v_bfe_u32 v7, v128, 16, 1
	v_add3_u32 v7, v128, v7, s86
	v_lshrrev_b32_e32 v7, 16, v7
	v_and_or_b32 v7, v8, s87, v7
	global_store_dwordx4 v[182:183], v[4:7], off offset:2048
	v_bfe_u32 v8, v133, 16, 1
	v_add3_u32 v8, v133, v8, s86
	v_bfe_u32 v4, v105, 16, 1
	v_add3_u32 v4, v105, v4, s86
	v_bfe_u32 v5, v109, 16, 1
	v_lshrrev_b32_e32 v4, 16, v4
	v_add3_u32 v5, v109, v5, s86
	v_and_or_b32 v4, v5, s87, v4
	v_bfe_u32 v5, v113, 16, 1
	v_add3_u32 v5, v113, v5, s86
	v_bfe_u32 v6, v117, 16, 1
	v_lshrrev_b32_e32 v5, 16, v5
	v_add3_u32 v6, v117, v6, s86
	v_and_or_b32 v5, v6, s87, v5
	v_bfe_u32 v6, v121, 16, 1
	v_add3_u32 v6, v121, v6, s86
	v_bfe_u32 v7, v125, 16, 1
	v_lshrrev_b32_e32 v6, 16, v6
	v_add3_u32 v7, v125, v7, s86
	v_and_or_b32 v6, v7, s87, v6
	v_bfe_u32 v7, v129, 16, 1
	v_add3_u32 v7, v129, v7, s86
	v_lshrrev_b32_e32 v7, 16, v7
	v_and_or_b32 v7, v8, s87, v7
	global_store_dwordx4 v[182:183], v[4:7], off offset:3072
	s_mov_b64 s[26:27], 0

.LBB0_736:
	v_xor_b32_e32 v4, 16, v242
	v_cmp_lt_i32_e32 vcc, v4, v17
	v_max_f32_e64 v5, |v102|, |v102|
	v_max_f32_e64 v6, |v107|, |v107|
	v_cndmask_b32_e32 v4, v242, v4, vcc
	v_lshlrev_b32_e32 v7, 2, v4
	v_max_f32_e64 v4, |v106|, |v106|
	v_max_f32_e32 v4, v5, v4
	v_max_f32_e64 v8, |v103|, |v103|
	v_max3_f32 v4, v4, |v110|, |v114|
	v_max_f32_e32 v6, v8, v6
	v_max3_f32 v4, v4, |v118|, |v122|
	v_max3_f32 v6, v6, |v111|, |v115|
	v_max3_f32 v4, v4, |v126|, |v130|
	v_max3_f32 v6, v6, |v119|, |v123|
	ds_bpermute_b32 v5, v7, v4
	v_max3_f32 v8, v6, |v127|, |v131|
	ds_bpermute_b32 v9, v7, v8
	v_max_f32_e64 v11, |v105|, |v105|
	s_waitcnt lgkmcnt(1)
	v_max_f32_e32 v5, v5, v5
	v_max_f32_e32 v4, v4, v5
	s_waitcnt lgkmcnt(0)
	v_max_f32_e32 v5, v9, v9
	v_max_f32_e32 v5, v8, v5
	v_max_f32_e64 v8, |v108|, |v108|
	v_max_f32_e64 v9, |v104|, |v104|
	v_max_f32_e32 v8, v9, v8
	v_max_f32_e64 v9, |v109|, |v109|
	v_max3_f32 v8, v8, |v112|, |v116|
	v_max_f32_e32 v9, v11, v9
	v_max3_f32 v8, v8, |v120|, |v124|
	v_max3_f32 v9, v9, |v113|, |v117|
	v_max3_f32 v8, v8, |v128|, |v132|
	v_max3_f32 v9, v9, |v121|, |v125|
	ds_bpermute_b32 v10, v7, v8
	v_max3_f32 v11, v9, |v129|, |v133|
	ds_bpermute_b32 v12, v7, v11
	ds_bpermute_b32 v6, v16, v4
	ds_bpermute_b32 v9, v16, v5
	s_waitcnt lgkmcnt(3)
	v_max_f32_e32 v7, v10, v10
	v_max_f32_e32 v7, v8, v7
	s_waitcnt lgkmcnt(2)
	v_max_f32_e32 v8, v12, v12
	v_max_f32_e32 v8, v11, v8
	ds_bpermute_b32 v10, v16, v7
	ds_bpermute_b32 v11, v16, v8
	s_and_saveexec_b64 s[10:11], s[8:9]
	s_cbranch_execz .LBB0_738
	s_waitcnt lgkmcnt(3)
	v_max_f32_e32 v6, v6, v6
	v_max_f32_e32 v4, v4, v4
	v_max_f32_e32 v4, v4, v6
	s_waitcnt lgkmcnt(2)
	v_max_f32_e32 v6, v9, v9
	v_max_f32_e32 v5, v5, v5
	v_max_f32_e32 v5, v5, v6
	s_waitcnt lgkmcnt(1)
	v_max_f32_e32 v6, v10, v10
	v_max_f32_e32 v7, v7, v7
	v_max_f32_e32 v6, v7, v6
	s_waitcnt lgkmcnt(0)
	v_max_f32_e32 v7, v11, v11
	v_max_f32_e32 v8, v8, v8
	v_max_f32_e32 v7, v8, v7
	global_atomic_smax v[186:187], v4, off
	global_atomic_smax v[186:187], v5, off offset:4
	global_atomic_smax v[186:187], v6, off offset:8
	global_atomic_smax v[186:187], v7, off offset:12

.LBB0_739:
	v_max_f32_e32 v4, v98, v98
	v_max_f32_e32 v4, 0xda24260, v4
	v_div_scale_f32 v5, s[10:11], v4, v4, s80
	s_waitcnt lgkmcnt(3)
	v_rcp_f32_e32 v6, v5
	s_nop 0
	v_fma_f32 v7, -v5, v6, 1.0
	v_fmac_f32_e32 v6, v7, v6
	v_div_scale_f32 v7, vcc, s80, v4, s80
	v_mul_f32_e32 v8, v7, v6
	s_waitcnt lgkmcnt(2)
	v_fma_f32 v9, -v5, v8, v7
	v_fmac_f32_e32 v8, v9, v6
	v_fma_f32 v5, -v5, v8, v7
	v_div_fmas_f32 v5, v5, v6, v8
	v_div_fixup_f32 v5, v5, v4, s80
	v_fmaak_f32 v4, v102, v5, 0x43000000
	v_cvt_pk_u8_f32 v4, v4, 0, 0
	v_fmaak_f32 v6, v106, v5, 0x43000000
	v_cvt_pk_u8_f32 v4, v6, 1, v4
	v_fmaak_f32 v6, v110, v5, 0x43000000
	v_cvt_pk_u8_f32 v4, v6, 2, v4
	v_fmaak_f32 v6, v114, v5, 0x43000000
	v_cvt_pk_u8_f32 v4, v6, 3, v4
	v_fmaak_f32 v6, v118, v5, 0x43000000
	v_cvt_pk_u8_f32 v6, v6, 0, 0
	v_fmaak_f32 v7, v122, v5, 0x43000000
	v_cvt_pk_u8_f32 v6, v7, 1, v6
	v_fmaak_f32 v7, v126, v5, 0x43000000
	v_cvt_pk_u8_f32 v6, v7, 2, v6
	v_fmaak_f32 v5, v130, v5, 0x43000000
	v_cvt_pk_u8_f32 v5, v5, 3, v6
	v_xor_b32_e32 v4, 0x80808080, v4
	v_xor_b32_e32 v5, 0x80808080, v5
	global_store_dwordx2 v[184:185], v[4:5], off
	v_max_f32_e32 v4, v99, v99
	v_max_f32_e32 v4, 0xda24260, v4
	v_div_scale_f32 v5, s[10:11], v4, v4, s80
	v_rcp_f32_e32 v6, v5
	s_nop 0
	v_fma_f32 v7, -v5, v6, 1.0
	v_fmac_f32_e32 v6, v7, v6
	v_div_scale_f32 v7, vcc, s80, v4, s80
	v_mul_f32_e32 v8, v7, v6
	v_fma_f32 v9, -v5, v8, v7
	v_fmac_f32_e32 v8, v9, v6
	v_fma_f32 v5, -v5, v8, v7
	v_div_fmas_f32 v5, v5, v6, v8
	v_div_fixup_f32 v5, v5, v4, s80
	v_fmaak_f32 v4, v103, v5, 0x43000000
	v_cvt_pk_u8_f32 v4, v4, 0, 0
	v_fmaak_f32 v6, v107, v5, 0x43000000
	v_cvt_pk_u8_f32 v4, v6, 1, v4
	v_fmaak_f32 v6, v111, v5, 0x43000000
	v_cvt_pk_u8_f32 v4, v6, 2, v4
	v_fmaak_f32 v6, v115, v5, 0x43000000
	v_cvt_pk_u8_f32 v4, v6, 3, v4
	v_fmaak_f32 v6, v119, v5, 0x43000000
	v_cvt_pk_u8_f32 v6, v6, 0, 0
	v_fmaak_f32 v7, v123, v5, 0x43000000
	v_cvt_pk_u8_f32 v6, v7, 1, v6
	v_fmaak_f32 v7, v127, v5, 0x43000000
	v_cvt_pk_u8_f32 v6, v7, 2, v6
	v_fmaak_f32 v5, v131, v5, 0x43000000
	v_cvt_pk_u8_f32 v5, v5, 3, v6
	v_xor_b32_e32 v4, 0x80808080, v4
	v_xor_b32_e32 v5, 0x80808080, v5
	global_store_dwordx2 v[184:185], v[4:5], off offset:1024
	v_max_f32_e32 v4, v100, v100
	v_max_f32_e32 v4, 0xda24260, v4
	v_div_scale_f32 v5, s[10:11], v4, v4, s80
	v_rcp_f32_e32 v6, v5
	s_nop 0
	v_fma_f32 v7, -v5, v6, 1.0
	v_fmac_f32_e32 v6, v7, v6
	v_div_scale_f32 v7, vcc, s80, v4, s80
	v_mul_f32_e32 v8, v7, v6
	v_fma_f32 v9, -v5, v8, v7
	v_fmac_f32_e32 v8, v9, v6
	v_fma_f32 v5, -v5, v8, v7
	v_div_fmas_f32 v5, v5, v6, v8
	v_div_fixup_f32 v5, v5, v4, s80
	v_fmaak_f32 v4, v104, v5, 0x43000000
	v_cvt_pk_u8_f32 v4, v4, 0, 0
	v_fmaak_f32 v6, v108, v5, 0x43000000
	v_cvt_pk_u8_f32 v4, v6, 1, v4
	v_fmaak_f32 v6, v112, v5, 0x43000000
	v_cvt_pk_u8_f32 v4, v6, 2, v4
	v_fmaak_f32 v6, v116, v5, 0x43000000
	v_cvt_pk_u8_f32 v4, v6, 3, v4
	v_fmaak_f32 v6, v120, v5, 0x43000000
	v_cvt_pk_u8_f32 v6, v6, 0, 0
	v_fmaak_f32 v7, v124, v5, 0x43000000
	v_cvt_pk_u8_f32 v6, v7, 1, v6
	v_fmaak_f32 v7, v128, v5, 0x43000000
	v_cvt_pk_u8_f32 v6, v7, 2, v6
	v_fmaak_f32 v5, v132, v5, 0x43000000
	v_cvt_pk_u8_f32 v5, v5, 3, v6
	v_xor_b32_e32 v4, 0x80808080, v4
	v_xor_b32_e32 v5, 0x80808080, v5
	global_store_dwordx2 v[184:185], v[4:5], off offset:2048
	v_max_f32_e32 v4, v101, v101
	v_max_f32_e32 v4, 0xda24260, v4
	v_div_scale_f32 v5, s[10:11], v4, v4, s80
	v_rcp_f32_e32 v6, v5
	s_nop 0
	v_fma_f32 v7, -v5, v6, 1.0
	v_fmac_f32_e32 v6, v7, v6
	v_div_scale_f32 v7, vcc, s80, v4, s80
	v_mul_f32_e32 v8, v7, v6
	v_fma_f32 v9, -v5, v8, v7
	v_fmac_f32_e32 v8, v9, v6
	v_fma_f32 v5, -v5, v8, v7
	v_div_fmas_f32 v5, v5, v6, v8
	v_div_fixup_f32 v5, v5, v4, s80
	v_fmaak_f32 v4, v105, v5, 0x43000000
	v_cvt_pk_u8_f32 v4, v4, 0, 0
	v_fmaak_f32 v6, v109, v5, 0x43000000
	v_cvt_pk_u8_f32 v4, v6, 1, v4
	v_fmaak_f32 v6, v113, v5, 0x43000000
	v_cvt_pk_u8_f32 v4, v6, 2, v4
	v_fmaak_f32 v6, v117, v5, 0x43000000
	v_cvt_pk_u8_f32 v4, v6, 3, v4
	v_fmaak_f32 v6, v121, v5, 0x43000000
	v_cvt_pk_u8_f32 v6, v6, 0, 0
	v_fmaak_f32 v7, v125, v5, 0x43000000
	v_cvt_pk_u8_f32 v6, v7, 1, v6
	v_fmaak_f32 v7, v129, v5, 0x43000000
	v_cvt_pk_u8_f32 v6, v7, 2, v6
	v_fmaak_f32 v5, v133, v5, 0x43000000
	v_cvt_pk_u8_f32 v5, v5, 3, v6
	v_xor_b32_e32 v4, 0x80808080, v4
	v_xor_b32_e32 v5, 0x80808080, v5
	global_store_dwordx2 v[184:185], v[4:5], off offset:3072
.Lbgstore_ret:
	s_cmp_eq_u32 s98, 0
	s_cbranch_scc1 .Lbg_hookret
	s_branch .Lbg_flushret

.LBB0_744:
	v_exp_f32_e32 v214, v16
	v_exp_f32_e32 v216, v17
	v_exp_f32_e32 v17, v84
	v_exp_f32_e32 v16, v85
	v_exp_f32_e32 v85, v86
	v_exp_f32_e32 v84, v87
	v_exp_f32_e32 v2, v82
	v_exp_f32_e32 v215, v83
	v_exp_f32_e32 v217, v66
	v_exp_f32_e32 v219, v67
	v_exp_f32_e32 v218, v68
	v_exp_f32_e32 v220, v69
	v_exp_f32_e32 v83, v70
	v_exp_f32_e32 v82, v71
	v_pk_mov_b32 v[68:69], v[16:17], v[16:17] op_sel:[1,0]
	v_pk_mov_b32 v[70:71], v[84:85], v[84:85] op_sel:[1,0]
	v_cvt_pk_bf16_f32 v66, v2, v215
	v_cvt_pk_bf16_f32 v67, v217, v219
	v_cvt_pk_bf16_f32 v68, v68, v69
	v_cvt_pk_bf16_f32 v69, v70, v71
	v_exp_f32_e32 v87, v88
	v_exp_f32_e32 v86, v89
	v_mfma_f32_32x32x16_bf16 v[34:49], v[174:177], v[66:69], v[34:49]
	v_exp_f32_e32 v89, v90
	v_exp_f32_e32 v88, v91
	v_exp_f32_e32 v91, v92
	v_exp_f32_e32 v90, v93
	v_exp_f32_e32 v93, v94
	v_exp_f32_e32 v92, v95
	v_exp_f32_e32 v97, v72
	v_exp_f32_e32 v96, v73
	v_pk_mov_b32 v[70:71], v[86:87], v[86:87] op_sel:[1,0]
	v_pk_mov_b32 v[72:73], v[88:89], v[88:89] op_sel:[1,0]
	v_exp_f32_e32 v195, v74
	v_exp_f32_e32 v194, v75
	v_cvt_pk_bf16_f32 v70, v70, v71
	v_cvt_pk_bf16_f32 v71, v72, v73
	v_pk_mov_b32 v[72:73], v[90:91], v[90:91] op_sel:[1,0]
	v_pk_mov_b32 v[74:75], v[92:93], v[92:93] op_sel:[1,0]
	v_cvt_pk_bf16_f32 v72, v72, v73
	v_cvt_pk_bf16_f32 v73, v74, v75
	v_mfma_f32_32x32x16_bf16 v[18:33], v[158:161], v[66:69], v[18:33]
	v_exp_f32_e32 v197, v76
	v_exp_f32_e32 v196, v77
	v_exp_f32_e32 v211, v78
	v_exp_f32_e32 v210, v79
	v_pk_mov_b32 v[76:77], v[82:83], v[82:83] op_sel:[1,0]
	v_pk_mov_b32 v[78:79], v[96:97], v[96:97] op_sel:[1,0]
	v_cvt_pk_bf16_f32 v74, v214, v216
	v_mfma_f32_32x32x16_bf16 v[34:49], v[170:173], v[70:73], v[34:49]
	v_cvt_pk_bf16_f32 v75, v218, v220
	v_cvt_pk_bf16_f32 v76, v76, v77
	v_cvt_pk_bf16_f32 v77, v78, v79
	v_exp_f32_e32 v213, v80
	v_exp_f32_e32 v212, v81
	v_pk_mov_b32 v[78:79], v[194:195], v[194:195] op_sel:[1,0]
	v_pk_mov_b32 v[80:81], v[196:197], v[196:197] op_sel:[1,0]
	v_mfma_f32_32x32x16_bf16 v[18:33], v[12:15], v[70:73], v[18:33]
	v_cvt_pk_bf16_f32 v78, v78, v79
	v_cvt_pk_bf16_f32 v79, v80, v81
	v_pk_mov_b32 v[80:81], v[210:211], v[210:211] op_sel:[1,0]
	v_pk_mov_b32 v[94:95], v[212:213], v[212:213] op_sel:[1,0]
	v_add_f32_e32 v2, v214, v2
	v_cvt_pk_bf16_f32 v80, v80, v81
	v_cvt_pk_bf16_f32 v81, v94, v95
	v_mfma_f32_32x32x16_bf16 v[34:49], v[166:169], v[74:77], v[34:49]
	v_add_f32_e32 v94, v216, v215
	v_add_f32_e32 v2, 0, v2
	v_add_f32_e32 v95, v218, v217
	v_add_f32_e32 v2, v94, v2
	v_add_f32_e32 v2, v95, v2
	v_pk_add_f32 v[16:17], v[82:83], v[16:17]
	v_pk_add_f32 v[66:67], v[96:97], v[84:85]
	v_mfma_f32_32x32x16_bf16 v[18:33], v[8:11], v[74:77], v[18:33]
	v_add_f32_e64 v68, v194, v86
	v_add_f32_e64 v69, v195, v87
	v_add_f32_e64 v82, v196, v88
	v_add_f32_e64 v83, v197, v89
	v_add_f32_e64 v84, v210, v90
	v_add_f32_e64 v85, v211, v91
	s_add_i32 s10, s60, 1
	v_pk_add_f32 v[86:87], v[212:213], v[92:93]
	s_and_b32 s60, s10, 3
	s_cmp_gt_u32 s99, 1
	s_cbranch_scc1 .Lbgw_m15
	s_waitcnt vmcnt(6) lgkmcnt(0)
	s_branch .Lbgw_mj

.Lbgw_mj:
	v_mfma_f32_32x32x16_bf16 v[34:49], v[162:165], v[78:81], v[34:49]
	v_add_f32_e32 v162, v220, v219
	v_add_f32_e32 v2, v162, v2
	v_add_f32_e32 v2, v17, v2
	v_add_f32_e32 v2, v16, v2
	v_add_f32_e32 v2, v67, v2
	v_add_f32_e32 v2, v66, v2
	v_add_f32_e32 v2, v69, v2
	v_add_f32_e32 v2, v68, v2
	v_mfma_f32_32x32x16_bf16 v[18:33], v[4:7], v[78:81], v[18:33]
	v_add_f32_e32 v2, v83, v2
	v_add_f32_e32 v2, v82, v2
	v_add_f32_e32 v2, v85, v2
	v_add_f32_e32 v2, v84, v2
	v_add_f32_e32 v2, v87, v2
	s_barrier
	s_add_i32 s10, s64, 1
	v_add_f32_e32 v2, v86, v2
	s_and_b32 s64, s10, 3
	s_add_i32 s35, s35, 1
	v_add_f32_e32 v191, v191, v2
	s_cmp_ge_i32 s35, s34
	v_add_u32_e32 v209, 64, v209
	s_cbranch_scc1 .LBB0_765

.LBB0_771:
	s_add_i32 s10, s60, 1
	s_and_b32 s60, s10, 3
	s_cmp_gt_u32 s99, 1
	s_cbranch_scc1 .Lbgw_d15
	s_waitcnt vmcnt(6) lgkmcnt(0)
	s_branch .Lbgw_dj

.Lbgw_dj:
	s_barrier
	s_add_i32 s10, s64, 1
	s_and_b32 s64, s10, 3
	s_add_i32 s71, s71, 1
	s_cmp_lt_i32 s71, s33
	s_cbranch_scc0 .LBB0_766

.LBB0_781:
	s_cmp_eq_u32 s99, 0
	s_cbranch_scc1 .Lbg_noflush
	s_waitcnt vmcnt(0)
	v_and_b32_e32 v4, 64, v242
	v_add_u32_e32 v17, 64, v4
	v_xor_b32_e32 v16, 32, v242
	v_cmp_lt_i32_e32 vcc, v16, v17
	s_nop 1
	v_cndmask_b32_e32 v2, v242, v16, vcc
	v_lshlrev_b32_e32 v16, 2, v2
	s_mov_b32 s99, 0
	s_mov_b32 s98, 1
	s_branch .Lbgstore
.Lbg_flushret:
	v_and_b32_e32 v2, 64, v242
	v_add_u32_e32 v2, 64, v2
